# attention loop: exact vmcnt in odd-step half (uniform counts via 16 same-line dummy loads on the last iteration)
# baseline (speedup 1.0000x reference)
.LBB0_1123:
	s_lshl_b32 s12, s35, 9
	s_add_i32 s12, s12, 0
	s_lshl_b32 s13, s34, 7
	s_add_i32 s12, s12, s13
	v_lshl_add_u32 v0, v232, 1, s12
	v_lshl_add_u32 v70, v233, 1, s12
	ds_read_u16 v14, v0 offset:32768
	ds_read_u16 v22, v0 offset:32800
	ds_read_u16 v30, v0 offset:32832
	ds_read_u16 v38, v0 offset:32864
	ds_read_u16 v46, v70 offset:32768
	ds_read_u16 v48, v70 offset:32784
	ds_read_u16 v62, v70 offset:32800
	ds_read_u16 v64, v70 offset:32816
	s_waitcnt lgkmcnt(7)
	v_lshlrev_b32_e32 v0, 9, v14
	v_lshl_add_u64 v[18:19], v[2:3], 0, v[0:1]
	s_waitcnt lgkmcnt(6)
	v_lshlrev_b32_e32 v0, 9, v22
	v_lshl_add_u64 v[26:27], v[2:3], 0, v[0:1]
	s_waitcnt lgkmcnt(5)
	v_lshlrev_b32_e32 v0, 9, v30
	v_lshl_add_u64 v[34:35], v[2:3], 0, v[0:1]
	s_waitcnt lgkmcnt(4)
	v_lshlrev_b32_e32 v0, 9, v38
	v_lshl_add_u64 v[42:43], v[2:3], 0, v[0:1]
	s_waitcnt lgkmcnt(3)
	v_lshlrev_b32_e32 v0, 9, v46
	v_lshl_add_u64 v[46:47], v[212:213], 0, v[0:1]
	s_waitcnt lgkmcnt(2)
	v_lshlrev_b32_e32 v0, 9, v48
	v_lshl_add_u64 v[50:51], v[212:213], 0, v[0:1]
	s_waitcnt lgkmcnt(1)
	v_lshlrev_b32_e32 v0, 9, v62
	v_lshl_add_u64 v[62:63], v[212:213], 0, v[0:1]
	s_waitcnt lgkmcnt(0)
	v_lshlrev_b32_e32 v0, 9, v64
	global_load_dwordx4 v[14:17], v[18:19], off
	s_nop 0
	global_load_dwordx4 v[18:21], v[18:19], off offset:64
	s_nop 0
	global_load_dwordx4 v[22:25], v[26:27], off
	s_nop 0
	global_load_dwordx4 v[26:29], v[26:27], off offset:64
	s_nop 0
	global_load_dwordx4 v[30:33], v[34:35], off
	s_nop 0
	global_load_dwordx4 v[34:37], v[34:35], off offset:64
	s_nop 0
	global_load_dwordx4 v[38:41], v[42:43], off
	s_nop 0
	global_load_dwordx4 v[42:45], v[42:43], off offset:64
	s_nop 0
	global_load_dwordx4 v[46:49], v[46:47], off offset:128
	s_nop 0
	global_load_dwordx4 v[50:53], v[50:51], off offset:128
	v_lshl_add_u64 v[66:67], v[212:213], 0, v[0:1]
	ds_read_u16 v0, v70 offset:32832
	global_load_dwordx4 v[62:65], v[62:63], off offset:128
	s_nop 0
	global_load_dwordx4 v[66:69], v[66:67], off offset:128
	ds_read_u16 v72, v70 offset:32848
	ds_read_u16 v78, v70 offset:32864
	ds_read_u16 v80, v70 offset:32880
	s_waitcnt lgkmcnt(3)
	v_lshlrev_b32_e32 v0, 9, v0
	v_lshl_add_u64 v[70:71], v[212:213], 0, v[0:1]
	s_waitcnt lgkmcnt(2)
	v_lshlrev_b32_e32 v0, 9, v72
	v_lshl_add_u64 v[74:75], v[212:213], 0, v[0:1]
	s_waitcnt lgkmcnt(1)
	v_lshlrev_b32_e32 v0, 9, v78
	v_lshl_add_u64 v[78:79], v[212:213], 0, v[0:1]
	s_waitcnt lgkmcnt(0)
	v_lshlrev_b32_e32 v0, 9, v80
	v_lshl_add_u64 v[82:83], v[212:213], 0, v[0:1]
	global_load_dwordx4 v[70:73], v[70:71], off offset:128
	s_nop 0
	global_load_dwordx4 v[74:77], v[74:75], off offset:128
	s_nop 0
	global_load_dwordx4 v[78:81], v[78:79], off offset:128
	s_nop 0
	global_load_dwordx4 v[82:85], v[82:83], off offset:128
	s_branch .LBB0_1124
.Lattn_dummy_b:
	global_load_dword v196, v[2:3], off
	global_load_dword v196, v[2:3], off
	global_load_dword v196, v[2:3], off
	global_load_dword v196, v[2:3], off
	global_load_dword v196, v[2:3], off
	global_load_dword v196, v[2:3], off
	global_load_dword v196, v[2:3], off
	global_load_dword v196, v[2:3], off
	global_load_dword v196, v[2:3], off
	global_load_dword v196, v[2:3], off
	global_load_dword v196, v[2:3], off
	global_load_dword v196, v[2:3], off
	global_load_dword v196, v[2:3], off
	global_load_dword v196, v[2:3], off
	global_load_dword v196, v[2:3], off
	global_load_dword v196, v[2:3], off

.LBB0_1138:
	s_waitcnt vmcnt(31)
	v_mfma_f32_16x16x32_bf16 v[138:141], v[138:141], v[6:9], v[150:153]
	v_add_f32_e32 v0, v182, v183
	s_mov_b32 s12, 0x40c00000
	s_waitcnt vmcnt(27)
	v_mfma_f32_16x16x32_bf16 v[130:133], v[130:133], v[6:9], v[174:177]
	s_waitcnt vmcnt(25) lgkmcnt(0)
	v_mfma_f32_16x16x32_bf16 v[122:125], v[122:125], v[6:9], v[178:181]
	v_mfma_f32_16x16x32_bf16 v[138:141], v[142:145], v[10:13], v[138:141]
	v_add_f32_e32 v142, v244, v0
	v_mfma_f32_16x16x32_bf16 v[144:147], v[146:149], v[6:9], v[170:173]
	v_mfma_f32_16x16x32_bf16 v[126:129], v[126:129], v[10:13], v[130:133]
	s_nop 4
	v_max_f32_e32 v0, v141, v141
	v_max_f32_e32 v143, v140, v140
	v_max_f32_e32 v0, v143, v0
	s_waitcnt vmcnt(24)
	v_mfma_f32_16x16x32_bf16 v[118:121], v[118:121], v[10:13], v[122:125]
	v_max3_f32 v0, v138, v139, v0
	v_max_f32_e32 v130, v127, v127
	v_max_f32_e32 v131, v126, v126
	v_mfma_f32_16x16x32_bf16 v[134:137], v[134:137], v[10:13], v[144:147]
	v_max_f32_e32 v130, v131, v130
	s_nop 2
	v_max_f32_e32 v122, v121, v121
	v_max_f32_e32 v123, v120, v120
	v_max_f32_e32 v131, v129, v129
	v_max_f32_e32 v132, v128, v128
	v_max_f32_e32 v143, v137, v137
	v_max_f32_e32 v144, v136, v136
	v_max_f32_e32 v122, v123, v122
	v_max_f32_e32 v143, v144, v143
	v_max_f32_e32 v131, v132, v131
	v_max3_f32 v122, v118, v119, v122
	v_max3_f32 v143, v134, v135, v143
	v_max3_f32 v122, v130, v131, v122
	v_max3_f32 v0, v0, v143, v122
	v_mov_b32_e32 v122, v0
	s_nop 1
	v_permlane16_swap_b32_e32 v0, v122
	v_max_f32_e32 v122, v122, v122
	v_max_f32_e32 v0, v0, v0
	v_max_f32_e32 v0, v0, v122
	v_mov_b32_e32 v122, v0
	s_nop 1
	v_permlane32_swap_b32_e32 v0, v122
	v_max_f32_e32 v122, v122, v122
	v_max_f32_e32 v0, v0, v0
	v_max_f32_e32 v0, v0, v122
	v_sub_f32_e32 v122, v0, v202
	v_mul_f32_e32 v122, 0x3e38aa3b, v122
	v_cmp_lt_f32_e32 vcc, s12, v122
	s_cbranch_vccz .LBB0_1140
	v_max_f32_e32 v0, v0, v0
	v_max_f32_e32 v122, v202, v202
	v_max_f32_e32 v143, v122, v0
	v_sub_f32_e32 v0, v202, v143
	v_mul_f32_e32 v0, 0x3e38aa3b, v0
	v_exp_f32_e32 v202, v0
	s_nop 0
	v_pk_mul_f32 v[186:187], v[142:143], v[202:203]
	v_pk_mul_f32 v[156:157], v[156:157], v[202:203] op_sel_hi:[1,0]
	v_pk_mul_f32 v[154:155], v[154:155], v[202:203] op_sel_hi:[1,0]
	v_pk_mul_f32 v[160:161], v[160:161], v[202:203] op_sel_hi:[1,0]
	v_pk_mul_f32 v[158:159], v[158:159], v[202:203] op_sel_hi:[1,0]
	v_pk_mul_f32 v[164:165], v[164:165], v[202:203] op_sel_hi:[1,0]
	v_pk_mul_f32 v[162:163], v[162:163], v[202:203] op_sel_hi:[1,0]
	v_pk_mul_f32 v[168:169], v[168:169], v[202:203] op_sel_hi:[1,0]
	v_pk_mul_f32 v[166:167], v[166:167], v[202:203] op_sel_hi:[1,0]
	v_mov_b32_e32 v202, v143
	v_mov_b32_e32 v142, v186
.LBB0_1140:
	v_fmamk_f32 v0, v138, 0x3e38aa3b, v187
	v_exp_f32_e32 v0, v0
	v_fmamk_f32 v122, v139, 0x3e38aa3b, v187
	v_exp_f32_e32 v122, v122
	v_fmamk_f32 v123, v140, 0x3e38aa3b, v187
	v_exp_f32_e32 v123, v123
	v_fmamk_f32 v124, v141, 0x3e38aa3b, v187
	v_exp_f32_e32 v124, v124
	v_fmamk_f32 v130, v134, 0x3e38aa3b, v187
	v_add_f32_e32 v125, 0, v0
	v_exp_f32_e32 v130, v130
	v_fmamk_f32 v131, v135, 0x3e38aa3b, v187
	v_add_f32_e32 v125, v122, v125
	v_exp_f32_e32 v131, v131
	v_fmamk_f32 v132, v136, 0x3e38aa3b, v187
	v_add_f32_e32 v125, v123, v125
	v_exp_f32_e32 v132, v132
	v_fmamk_f32 v133, v137, 0x3e38aa3b, v187
	v_add_f32_e32 v125, v124, v125
	v_exp_f32_e32 v133, v133
	v_fmamk_f32 v126, v126, 0x3e38aa3b, v187
	v_add_f32_e32 v125, v130, v125
	v_exp_f32_e32 v126, v126
	v_fmamk_f32 v127, v127, 0x3e38aa3b, v187
	v_add_f32_e32 v125, v131, v125
	v_exp_f32_e32 v127, v127
	v_fmamk_f32 v128, v128, 0x3e38aa3b, v187
	v_add_f32_e32 v125, v132, v125
	v_exp_f32_e32 v128, v128
	v_fmamk_f32 v129, v129, 0x3e38aa3b, v187
	v_add_f32_e32 v125, v133, v125
	v_exp_f32_e32 v129, v129
	v_fmamk_f32 v118, v118, 0x3e38aa3b, v187
	v_add_f32_e32 v125, v126, v125
	v_exp_f32_e32 v134, v118
	v_fmamk_f32 v118, v119, 0x3e38aa3b, v187
	v_add_f32_e32 v125, v127, v125
	v_exp_f32_e32 v135, v118
	v_fmamk_f32 v118, v120, 0x3e38aa3b, v187
	v_add_f32_e32 v125, v128, v125
	v_exp_f32_e32 v136, v118
	v_fmac_f32_e32 v187, 0x3e38aa3b, v121
	v_add_f32_e32 v125, v129, v125
	v_exp_f32_e32 v137, v187
	v_add_f32_e32 v118, v134, v125
	v_add_f32_e32 v118, v135, v118
	v_add_f32_e32 v118, v136, v118
	v_add_f32_e32 v118, v137, v118
	v_mov_b32_e32 v119, v118
	s_nor_b64 s[12:13], s[26:27], s[30:31]
	s_nop 0
	v_permlane16_swap_b32_e32 v118, v119
	v_add_f32_e32 v125, v118, v119
	v_mov_b32_e32 v138, v125
	s_waitcnt vmcnt(23)
	ds_write_b128 v235, v[102:105]
	s_waitcnt vmcnt(22)
	ds_write_b128 v235, v[106:109] offset:1024
	s_waitcnt vmcnt(21)
	ds_write_b128 v235, v[110:113] offset:2048
	s_waitcnt vmcnt(20)
	ds_write_b128 v235, v[114:117] offset:3072
	v_cvt_pk_bf16_f32 v102, v0, v122
	v_cvt_pk_bf16_f32 v103, v123, v124
	v_cvt_pk_bf16_f32 v104, v130, v131
	v_cvt_pk_bf16_f32 v105, v132, v133
	ds_read_b64_tr_b16 v[106:107], v236
	ds_read_b64_tr_b16 v[108:109], v237
	ds_read_b64_tr_b16 v[110:111], v238
	ds_read_b64_tr_b16 v[112:113], v239
	ds_read_b64_tr_b16 v[114:115], v240
	ds_read_b64_tr_b16 v[116:117], v241
	ds_read_b64_tr_b16 v[118:119], v242
	ds_read_b64_tr_b16 v[120:121], v243
	s_waitcnt vmcnt(19)
	ds_write_b128 v235, v[86:89]
	s_waitcnt vmcnt(18)
	ds_write_b128 v235, v[90:93] offset:1024
	s_waitcnt vmcnt(17)
	ds_write_b128 v235, v[94:97] offset:2048
	s_waitcnt vmcnt(16)
	ds_write_b128 v235, v[98:101] offset:3072
	v_cvt_pk_bf16_f32 v86, v126, v127
	v_cvt_pk_bf16_f32 v87, v128, v129
	v_cvt_pk_bf16_f32 v88, v134, v135
	v_cvt_pk_bf16_f32 v89, v136, v137
	ds_read_b64_tr_b16 v[90:91], v236
	ds_read_b64_tr_b16 v[92:93], v237
	ds_read_b64_tr_b16 v[98:99], v238
	ds_read_b64_tr_b16 v[100:101], v239
	s_waitcnt lgkmcnt(14)
	v_mfma_f32_16x16x32_bf16 v[106:109], v[106:109], v[102:105], v[154:157]
	v_permlane32_swap_b32_e32 v125, v138
	v_add_f32_e32 v0, v125, v138
	s_waitcnt lgkmcnt(12)
	v_mfma_f32_16x16x32_bf16 v[110:113], v[110:113], v[102:105], v[158:161]
	v_add_f32_e32 v244, v142, v0
	s_waitcnt lgkmcnt(10)
	v_mfma_f32_16x16x32_bf16 v[114:117], v[114:117], v[102:105], v[162:165]
	s_waitcnt lgkmcnt(8)
	v_mfma_f32_16x16x32_bf16 v[94:97], v[118:121], v[102:105], v[166:169]
	s_waitcnt lgkmcnt(2)
	v_mfma_f32_16x16x32_bf16 v[166:169], v[90:93], v[86:89], v[106:109]
	ds_read_b64_tr_b16 v[90:91], v240
	ds_read_b64_tr_b16 v[92:93], v241
	s_waitcnt lgkmcnt(2)
	v_mfma_f32_16x16x32_bf16 v[162:165], v[98:101], v[86:89], v[110:113]
	ds_read_b64_tr_b16 v[98:99], v242
	ds_read_b64_tr_b16 v[100:101], v243
	s_waitcnt lgkmcnt(2)
	v_mfma_f32_16x16x32_bf16 v[158:161], v[90:93], v[86:89], v[114:117]
	s_waitcnt lgkmcnt(0)
	v_mfma_f32_16x16x32_bf16 v[154:157], v[98:101], v[86:89], v[94:97]
	s_and_saveexec_b64 s[34:35], s[12:13]
	s_xor_b64 s[12:13], exec, s[34:35]
	s_cbranch_execz .LBB0_1142
	v_div_scale_f32 v0, s[34:35], v244, v244, 1.0
	v_rcp_f32_e32 v6, v0
	s_ashr_i32 s35, s42, 31
	v_div_scale_f32 v7, vcc, 1.0, v244, 1.0
	v_fma_f32 v8, -v0, v6, 1.0
	v_fmac_f32_e32 v6, v8, v6
	s_add_u32 s34, s0, s42
	v_mul_f32_e32 v8, v7, v6
	s_addc_u32 s35, s1, s35
	v_fma_f32 v9, -v0, v8, v7
	s_lshl_b64 s[34:35], s[34:35], 11
	v_fmac_f32_e32 v8, v9, v6
	s_add_u32 s34, s60, s34
	v_fma_f32 v0, -v0, v8, v7
	s_addc_u32 s35, s61, s35
	v_mov_b32_e32 v217, v1
	v_div_fmas_f32 v0, v0, v6, v8
	v_lshl_add_u64 v[6:7], s[34:35], 0, v[216:217]
	v_lshl_add_u64 v[6:7], v[210:211], 1, v[6:7]
	s_mov_b64 s[16:17], 0x13c00200
	v_div_fixup_f32 v0, v0, v244, 1.0
	v_lshl_add_u64 v[8:9], v[6:7], 0, s[16:17]
	s_mov_b32 s16, 0x13c00000
	v_mul_f32_e32 v10, v0, v166
	v_mul_f32_e32 v11, v0, v167
	v_add_co_u32_e32 v6, vcc, s16, v6
	v_cvt_pk_bf16_f32 v10, v10, v11
	v_mul_f32_e32 v11, v0, v168
	s_nop 0
	v_addc_co_u32_e32 v7, vcc, 0, v7, vcc
	v_mul_f32_e32 v12, v0, v169
	v_cvt_pk_bf16_f32 v11, v11, v12
	global_store_dwordx2 v[6:7], v[10:11], off offset:512
	v_mul_f32_e32 v6, v0, v162
	v_mul_f32_e32 v7, v0, v163
	v_cvt_pk_bf16_f32 v6, v6, v7
	v_mul_f32_e32 v7, v0, v164
	v_mul_f32_e32 v10, v0, v165
	v_cvt_pk_bf16_f32 v7, v7, v10
	global_store_dwordx2 v[8:9], v[6:7], off offset:32
	v_mul_f32_e32 v6, v0, v158
	v_mul_f32_e32 v7, v0, v159
	v_cvt_pk_bf16_f32 v6, v6, v7
	v_mul_f32_e32 v7, v0, v160
	v_mul_f32_e32 v10, v0, v161
	v_cvt_pk_bf16_f32 v7, v7, v10
	global_store_dwordx2 v[8:9], v[6:7], off offset:64
	v_mul_f32_e32 v6, v0, v154
	v_mul_f32_e32 v7, v0, v155
	v_cvt_pk_bf16_f32 v6, v6, v7
	v_mul_f32_e32 v7, v0, v156
	v_mul_f32_e32 v0, v0, v157
	v_cvt_pk_bf16_f32 v7, v7, v0
	global_store_dwordx2 v[8:9], v[6:7], off offset:96

.LBB0_1144:
	s_waitcnt vmcnt(0)
	s_waitcnt lgkmcnt(0)
	s_barrier
	s_cbranch_execz .LBB0_798
	s_branch .LBB0_829
